# P3 side tables: per-row wave max by DPP scan + readlane instead of 6 serial ds_bpermute round trips
# baseline (speedup 1.0000x reference)
; #define LAS __attribute__((address_space(3)))
; __device__ __forceinline__ void p3_side_tables(const Params& P, LAS unsigned char* lds, int tid, int lane, int wave, int sb, int nsb) {
;     ...
;         float mx = 0.f, sq = 0.f;
; #pragma unroll
;         for (int j = 0; j < 4; ++j)
; #pragma unroll
;             for (int i = 0; i < 4; ++i) { mx = fmaxf(mx, fabsf(v[j][i])); sq += v[j][i] * v[j][i]; }
;         mx = wave_max(mx);
;         unsigned w0 = 0u, w1 = 0u; float sc;
;         {
;             sc = mx > 0.f ? mx * (1.0f / 6.0f) : 1.0f; const float inv = 1.0f / sc;
;             w0 = __builtin_amdgcn_cvt_scalef32_pk_fp4_f32(w0, v[0][0] * inv, v[0][1] * inv, 1.0f, 0); w0 = __builtin_amdgcn_cvt_scalef32_pk_fp4_f32(w0, v[0][2] * inv, v[0][3] * inv, 1.0f, 1);
;             w0 = __builtin_amdgcn_cvt_scalef32_pk_fp4_f32(w0, v[1][0] * inv, v[1][1] * inv, 1.0f, 2); w0 = __builtin_amdgcn_cvt_scalef32_pk_fp4_f32(w0, v[1][2] * inv, v[1][3] * inv, 1.0f, 3);
;             w1 = __builtin_amdgcn_cvt_scalef32_pk_fp4_f32(w1, v[2][0] * inv, v[2][1] * inv, 1.0f, 0); w1 = __builtin_amdgcn_cvt_scalef32_pk_fp4_f32(w1, v[2][2] * inv, v[2][3] * inv, 1.0f, 1);
;             w1 = __builtin_amdgcn_cvt_scalef32_pk_fp4_f32(w1, v[3][0] * inv, v[3][1] * inv, 1.0f, 2); w1 = __builtin_amdgcn_cvt_scalef32_pk_fp4_f32(w1, v[3][2] * inv, v[3][3] * inv, 1.0f, 3);
;         }
;         unsigned* dst = (unsigned*)(ws + (tb_ ? WS_V4 : WS_U4)) + (size_t)(lane >> 5) * 524288 + (size_t)e * 32 + (lane & 31);
;         if (tb_) {
;             LAS unsigned char* sb = (LAS unsigned char*)scr; const int l5 = lane & 31, s0 = (lane >> 5) * 128, bp = 32 * (l5 & 3) + (l5 >> 2);
;             asm volatile("s_waitcnt lgkmcnt(0)" ::: "memory");
; #pragma unroll
;             for (int b = 0; b < 4; ++b) { sb[s0 + bp + 8 * b] = (unsigned char)(w0 >> (8 * b)); sb[256 + s0 + bp + 8 * b] = (unsigned char)(w1 >> (8 * b)); }
;             asm volatile("s_waitcnt lgkmcnt(0)" ::: "memory");
;             w0 = *(LAS unsigned*)(sb + 4 * lane); w1 = *(LAS unsigned*)(sb + 256 + 4 * lane);
.LBB0_576:
	v_max3_f32 v86, |v42|, 0, |v43|
	v_max3_f32 v86, v86, |v44|, |v45|
	v_max3_f32 v86, v86, |v34|, |v35|
	v_max3_f32 v86, v86, |v36|, |v37|
	v_max3_f32 v86, v86, |v46|, |v47|
	v_max3_f32 v86, v86, |v48|, |v49|
	v_max3_f32 v86, v86, |v38|, |v39|
	v_max3_f32 v86, v86, |v40|, |v41|
	s_nop 1
	v_max_f32_dpp v86, v86, v86 row_shr:1 row_mask:0xf bank_mask:0xf
	s_nop 1
	v_max_f32_dpp v86, v86, v86 row_shr:2 row_mask:0xf bank_mask:0xf
	s_nop 1
	v_max_f32_dpp v86, v86, v86 row_shr:4 row_mask:0xf bank_mask:0xf
	s_nop 1
	v_max_f32_dpp v86, v86, v86 row_shr:8 row_mask:0xf bank_mask:0xf
	s_nop 1
	v_max_f32_dpp v86, v86, v86 row_bcast:15 row_mask:0xa bank_mask:0xf
	s_nop 1
	v_max_f32_dpp v86, v86, v86 row_bcast:31 row_mask:0xc bank_mask:0xf
	s_nop 0
	v_readlane_b32 s98, v86, 63
	v_mov_b32_e32 v86, 0
	v_mov_b32_e32 v87, 0
	v_mov_b32_e32 v96, s98
	v_mul_f32_e32 v97, 0x3e2aaaab, v96
	v_cmp_lt_f32_e32 vcc, 0, v96
	s_nop 1
	v_cndmask_b32_e32 v96, 1.0, v97, vcc
	v_div_scale_f32 v97, s[24:25], v96, v96, 1.0
	v_rcp_f32_e32 v98, v97
	v_div_scale_f32 v99, vcc, 1.0, v96, 1.0
	v_fma_f32 v100, -v97, v98, 1.0
	v_fmac_f32_e32 v98, v100, v98
	v_mul_f32_e32 v100, v99, v98
	v_fma_f32 v101, -v97, v100, v99
	v_fmac_f32_e32 v100, v101, v98
	v_fma_f32 v97, -v97, v100, v99
	v_div_fmas_f32 v97, v97, v98, v100
	v_div_fixup_f32 v97, v97, v96, 1.0
	v_mul_f32_e32 v42, v42, v97
	v_mul_f32_e32 v43, v43, v97
	v_mul_f32_e32 v46, v46, v97
	v_mul_f32_e32 v47, v47, v97
	v_mul_f32_e32 v44, v44, v97
	v_mul_f32_e32 v45, v45, v97
	v_mul_f32_e32 v48, v48, v97
	v_mul_f32_e32 v49, v49, v97
	v_cvt_scalef32_pk_fp4_f32 v86, v42, v43, 1.0
	v_cvt_scalef32_pk_fp4_f32 v87, v46, v47, 1.0
	v_mul_f32_e32 v34, v34, v97
	v_mul_f32_e32 v35, v35, v97
	v_mul_f32_e32 v38, v38, v97
	v_mul_f32_e32 v39, v39, v97
	v_cvt_scalef32_pk_fp4_f32 v86, v44, v45, 1.0 op_sel:[0,0,1,0]
	v_cvt_scalef32_pk_fp4_f32 v87, v48, v49, 1.0 op_sel:[0,0,1,0]
	v_mul_f32_e32 v36, v36, v97
	v_mul_f32_e32 v37, v37, v97
	v_mul_f32_e32 v40, v40, v97
	v_mul_f32_e32 v41, v41, v97
	v_cvt_scalef32_pk_fp4_f32 v86, v34, v35, 1.0 op_sel:[0,0,0,1]
	v_cvt_scalef32_pk_fp4_f32 v87, v38, v39, 1.0 op_sel:[0,0,0,1]
	v_cvt_scalef32_pk_fp4_f32 v86, v36, v37, 1.0 op_sel:[0,0,1,1]
	s_andn2_b64 vcc, exec, s[6:7]
	v_cvt_scalef32_pk_fp4_f32 v87, v40, v41, 1.0 op_sel:[0,0,1,1]
	s_cbranch_vccnz .LBB0_578
	v_lshrrev_b32_e32 v34, 8, v86
	s_waitcnt lgkmcnt(0)
	ds_write_b8 v94, v86
	ds_write_b8 v94, v87 offset:256
	ds_write_b8 v94, v34 offset:8
	v_lshrrev_b32_e32 v34, 8, v87
	ds_write_b8 v94, v34 offset:264
	ds_write_b8_d16_hi v94, v86 offset:16
	ds_write_b8_d16_hi v94, v87 offset:272
	v_lshrrev_b32_e32 v34, 24, v86
	ds_write_b8 v94, v34 offset:24
	v_lshrrev_b32_e32 v34, 24, v87
	ds_write_b8 v94, v34 offset:280
	s_waitcnt lgkmcnt(0)
	ds_read2st64_b32 v[86:87], v95 offset1:1
	s_waitcnt lgkmcnt(0)
